# PREP1 rope-key mini-GEMM: second tasks moved from workgroups 0-15 to 240-255 (which have one G2 unit less); plus static prio
# speedup vs baseline: 1.0184x; 1.0184x over previous
.LBB0_374:
	s_mov_b64 s[6:7], s[34:35]
	v_readfirstlane_b32 s0, v169
	s_mov_b32 s5, s14
	s_mov_b32 s4, s15
	s_not_b32 s98, s5
	s_add_i32 s98, s98, s4
	s_ashr_i32 s10, s0, 6
	s_add_u32 s8, s6, 0x3c01c000
	v_and_b32_e32 v54, 63, v169
	s_addc_u32 s9, s7, 0
	s_cmpk_gt_i32 s98, 0x10f
	v_lshlrev_b32_e32 v55, 6, v54
	s_cbranch_scc1 .LBB0_377
	v_and_b32_e32 v56, 15, v169
	s_lshl_b32 s0, s10, 8
	v_mov_b32_e32 v1, 0
	s_ashr_i32 s1, s0, 31
	v_lshlrev_b32_e32 v4, 12, v56
	v_mov_b32_e32 v5, v1
	s_lshl_b64 s[0:1], s[0:1], 1
	v_lshl_add_u64 v[4:5], s[6:7], 0, v[4:5]
	s_add_u32 s2, s6, s0
	v_and_b32_e32 v0, 48, v169
	v_lshl_add_u64 v[4:5], v[4:5], 0, s[0:1]
	s_addc_u32 s3, s7, s1
	v_lshl_add_u64 v[52:53], v[4:5], 0, v[0:1]
	s_mov_b64 s[0:1], 0x2658000
	v_lshl_add_u64 v[4:5], v[52:53], 0, s[0:1]
	s_mov_b64 s[0:1], 0x2668000
	v_lshl_add_u64 v[6:7], v[52:53], 0, s[0:1]
	s_mov_b64 s[0:1], 0x2668040
	v_lshl_add_u64 v[8:9], v[52:53], 0, s[0:1]
	s_mov_b64 s[0:1], 0x2668080
	v_lshl_add_u64 v[10:11], v[52:53], 0, s[0:1]
	s_mov_b64 s[0:1], 0x26680c0
	v_lshl_add_u64 v[12:13], v[52:53], 0, s[0:1]
	s_mov_b64 s[0:1], 0x2668100
	v_lshl_add_u64 v[14:15], v[52:53], 0, s[0:1]
	s_mov_b64 s[0:1], 0x2668140
	v_lshl_add_u64 v[16:17], v[52:53], 0, s[0:1]
	s_mov_b64 s[0:1], 0x2668180
	v_lshl_add_u64 v[18:19], v[52:53], 0, s[0:1]
	s_mov_b64 s[0:1], 0x26681c0
	v_lshl_add_u64 v[20:21], v[52:53], 0, s[0:1]
	s_mov_b64 s[0:1], 0x2678000
	v_lshl_add_u64 v[22:23], v[52:53], 0, s[0:1]
	s_mov_b64 s[0:1], 0x2678040
	v_lshl_add_u64 v[24:25], v[52:53], 0, s[0:1]
	s_mov_b64 s[0:1], 0x2678080
	v_lshl_add_u64 v[26:27], v[52:53], 0, s[0:1]
	s_mov_b64 s[0:1], 0x26780c0
	v_lshl_add_u64 v[28:29], v[52:53], 0, s[0:1]
	s_mov_b64 s[0:1], 0x2678100
	v_lshl_add_u64 v[30:31], v[52:53], 0, s[0:1]
	s_mov_b64 s[0:1], 0x2678140
	v_lshl_add_u64 v[32:33], v[52:53], 0, s[0:1]
	s_mov_b64 s[0:1], 0x2678180
	v_lshl_add_u64 v[34:35], v[52:53], 0, s[0:1]
	s_mov_b64 s[0:1], 0x26781c0
	v_lshl_add_u64 v[36:37], v[52:53], 0, s[0:1]
	s_mov_b64 s[0:1], 0x2688000
	v_lshl_add_u64 v[38:39], v[52:53], 0, s[0:1]
	s_mov_b64 s[0:1], 0x2688040
	v_lshl_add_u64 v[40:41], v[52:53], 0, s[0:1]
	s_mov_b64 s[0:1], 0x2688080
	v_lshl_add_u64 v[42:43], v[52:53], 0, s[0:1]
	s_mov_b64 s[0:1], 0x26880c0
	v_lshl_add_u64 v[44:45], v[52:53], 0, s[0:1]
	s_mov_b64 s[0:1], 0x2688100
	v_lshl_add_u64 v[46:47], v[52:53], 0, s[0:1]
	s_mov_b64 s[0:1], 0x2688140
	v_lshl_add_u64 v[48:49], v[52:53], 0, s[0:1]
	s_mov_b64 s[0:1], 0x2688180
	v_lshl_add_u64 v[50:51], v[52:53], 0, s[0:1]
	s_mov_b64 s[0:1], 0x26881c0
	v_lshl_add_u64 v[52:53], v[52:53], 0, s[0:1]
	s_lshl_b32 s0, s10, 13
	s_waitcnt lgkmcnt(0)
	v_lshl_add_u64 v[2:3], s[2:3], 0, v[0:1]
	s_add_i32 s0, s0, 0
	v_and_b32_e32 v0, 0xc00, v55
	v_lshlrev_b32_e32 v59, 2, v56
	v_add3_u32 v57, s0, v0, v59
	v_and_b32_e32 v0, 0xf00, v55
	v_or_b32_e32 v58, 0x300, v0
	v_or_b32_e32 v0, 0x1300, v0
	v_add3_u32 v58, s0, v58, v59
	v_add3_u32 v59, s0, v0, v59
	v_lshlrev_b32_e32 v0, 2, v169
	v_ashrrev_i32_e32 v60, 4, v169
	v_and_b32_e32 v0, 60, v0
	s_mov_b64 s[2:3], 0x1f4b8000
	v_lshlrev_b32_e32 v61, 8, v60
	v_lshlrev_b32_e32 v62, 2, v0
	v_lshl_add_u64 v[2:3], v[2:3], 0, s[2:3]
	v_add3_u32 v61, 0, v61, v62
	s_lshl_b32 s0, s98, 5
	s_lshl_b32 s1, s4, 5
	s_movk_i32 s2, 0x4c00
	v_lshlrev_b32_e32 v0, 1, v0
	s_mov_b32 s3, s98

.LBB0_1689:
	s_mov_b32 s4, s15
	v_readfirstlane_b32 s0, v169
	s_mov_b64 s[6:7], s[34:35]
	s_mov_b32 s5, s14
	s_not_b32 s98, s5
	s_add_i32 s98, s98, s4
	s_ashr_i32 s10, s0, 6
	s_add_u32 s8, s6, 0x3c01c000
	v_and_b32_e32 v54, 63, v169
	s_addc_u32 s9, s7, 0
	s_cmpk_gt_i32 s98, 0x10f
	v_lshlrev_b32_e32 v55, 6, v54
	s_cbranch_scc1 .LBB0_1692
	v_and_b32_e32 v56, 15, v169
	s_lshl_b32 s0, s10, 8
	v_mov_b32_e32 v1, 0
	s_ashr_i32 s1, s0, 31
	s_waitcnt lgkmcnt(0)
	v_lshlrev_b32_e32 v4, 12, v56
	v_mov_b32_e32 v5, v1
	s_lshl_b64 s[0:1], s[0:1], 1
	v_lshl_add_u64 v[4:5], s[6:7], 0, v[4:5]
	s_add_u32 s2, s6, s0
	v_and_b32_e32 v0, 48, v169
	v_lshl_add_u64 v[4:5], v[4:5], 0, s[0:1]
	s_addc_u32 s3, s7, s1
	v_lshl_add_u64 v[52:53], v[4:5], 0, v[0:1]
	s_mov_b64 s[0:1], 0x4c58000
	v_lshl_add_u64 v[4:5], v[52:53], 0, s[0:1]
	s_mov_b64 s[0:1], 0x4c68000
	v_lshl_add_u64 v[6:7], v[52:53], 0, s[0:1]
	s_mov_b64 s[0:1], 0x4c68040
	v_lshl_add_u64 v[8:9], v[52:53], 0, s[0:1]
	s_mov_b64 s[0:1], 0x4c68080
	v_lshl_add_u64 v[10:11], v[52:53], 0, s[0:1]
	s_mov_b64 s[0:1], 0x4c680c0
	v_lshl_add_u64 v[12:13], v[52:53], 0, s[0:1]
	s_mov_b64 s[0:1], 0x4c68100
	v_lshl_add_u64 v[14:15], v[52:53], 0, s[0:1]
	s_mov_b64 s[0:1], 0x4c68140
	v_lshl_add_u64 v[16:17], v[52:53], 0, s[0:1]
	s_mov_b64 s[0:1], 0x4c68180
	v_lshl_add_u64 v[18:19], v[52:53], 0, s[0:1]
	s_mov_b64 s[0:1], 0x4c681c0
	v_lshl_add_u64 v[20:21], v[52:53], 0, s[0:1]
	s_mov_b64 s[0:1], 0x4c78000
	v_lshl_add_u64 v[22:23], v[52:53], 0, s[0:1]
	s_mov_b64 s[0:1], 0x4c78040
	v_lshl_add_u64 v[24:25], v[52:53], 0, s[0:1]
	s_mov_b64 s[0:1], 0x4c78080
	v_lshl_add_u64 v[26:27], v[52:53], 0, s[0:1]
	s_mov_b64 s[0:1], 0x4c780c0
	v_lshl_add_u64 v[28:29], v[52:53], 0, s[0:1]
	s_mov_b64 s[0:1], 0x4c78100
	v_lshl_add_u64 v[30:31], v[52:53], 0, s[0:1]
	s_mov_b64 s[0:1], 0x4c78140
	v_lshl_add_u64 v[32:33], v[52:53], 0, s[0:1]
	s_mov_b64 s[0:1], 0x4c78180
	v_lshl_add_u64 v[34:35], v[52:53], 0, s[0:1]
	s_mov_b64 s[0:1], 0x4c781c0
	v_lshl_add_u64 v[36:37], v[52:53], 0, s[0:1]
	s_mov_b64 s[0:1], 0x4c88000
	v_lshl_add_u64 v[38:39], v[52:53], 0, s[0:1]
	s_mov_b64 s[0:1], 0x4c88040
	v_lshl_add_u64 v[40:41], v[52:53], 0, s[0:1]
	s_mov_b64 s[0:1], 0x4c88080
	v_lshl_add_u64 v[42:43], v[52:53], 0, s[0:1]
	s_mov_b64 s[0:1], 0x4c880c0
	v_lshl_add_u64 v[44:45], v[52:53], 0, s[0:1]
	s_mov_b64 s[0:1], 0x4c88100
	v_lshl_add_u64 v[46:47], v[52:53], 0, s[0:1]
	s_mov_b64 s[0:1], 0x4c88140
	v_lshl_add_u64 v[48:49], v[52:53], 0, s[0:1]
	s_mov_b64 s[0:1], 0x4c88180
	v_lshl_add_u64 v[50:51], v[52:53], 0, s[0:1]
	s_mov_b64 s[0:1], 0x4c881c0
	v_lshl_add_u64 v[52:53], v[52:53], 0, s[0:1]
	s_lshl_b32 s0, s10, 13
	v_lshl_add_u64 v[2:3], s[2:3], 0, v[0:1]
	s_add_i32 s0, s0, 0
	v_and_b32_e32 v0, 0xc00, v55
	v_lshlrev_b32_e32 v59, 2, v56
	v_add3_u32 v57, s0, v0, v59
	v_and_b32_e32 v0, 0xf00, v55
	v_or_b32_e32 v58, 0x300, v0
	v_or_b32_e32 v0, 0x1300, v0
	v_add3_u32 v58, s0, v58, v59
	v_add3_u32 v59, s0, v0, v59
	v_lshlrev_b32_e32 v0, 2, v169
	v_ashrrev_i32_e32 v60, 4, v169
	v_and_b32_e32 v0, 60, v0
	s_mov_b64 s[2:3], 0x1f4b8000
	v_lshlrev_b32_e32 v61, 8, v60
	v_lshlrev_b32_e32 v62, 2, v0
	v_lshl_add_u64 v[2:3], v[2:3], 0, s[2:3]
	v_add3_u32 v61, 0, v61, v62
	s_lshl_b32 s0, s98, 5
	s_lshl_b32 s1, s4, 5
	s_movk_i32 s2, 0x4c00
	v_lshlrev_b32_e32 v0, 1, v0
	s_mov_b32 s3, s98
